# v12
# speedup vs baseline: 1.0153x; 1.0153x over previous
_Z12pool3_kernelPKfS0_Pf:
	s_load_dwordx4 s[4:7], s[0:1], 0x0
	s_load_dwordx2 s[8:9], s[0:1], 0x10
	v_and_b32_e32 v1, 63, v0
	v_lshrrev_b32_e32 v2, 6, v0
	v_lshlrev_b32_e32 v3, 5, v1
	v_lshlrev_b32_e32 v4, 4, v1
	s_lshl_b32 s12, s2, 14
	s_lshl_b32 s13, s2, 6
	v_lshl_add_u32 v5, v2, 12, v4
	v_add_u32_e32 v5, s12, v5
	v_lshlrev_b32_e32 v6, 9, v1
	v_lshl_add_u32 v6, v2, 4, v6
	v_add_u32_e32 v6, s13, v6
	v_add_u32_e32 v7, 0x8000, v6
	v_lshlrev_b32_e32 v8, 2, v1
	s_waitcnt lgkmcnt(0)
	s_add_u32 s10, s4, 0x20000
	s_addc_u32 s11, s5, 0
	global_load_dwordx4 v[10:13], v3, s[10:11]
	global_load_dwordx4 v[14:17], v3, s[10:11] offset:16
	global_load_dwordx4 v[20:23], v5, s[4:5]
	global_load_dwordx4 v[24:27], v5, s[4:5] offset:1024
	global_load_dwordx4 v[28:31], v5, s[4:5] offset:2048
	global_load_dwordx4 v[32:35], v5, s[4:5] offset:3072
	global_load_dwordx4 v[36:39], v6, s[6:7]
	global_load_dwordx4 v[40:43], v7, s[6:7]
	s_waitcnt vmcnt(6)
	v_max_f32_e32 v44, v10, v12
	v_max_f32_e32 v45, v14, v16
	v_max_f32_e32 v44, v44, v45
	s_nop 1
	v_max_f32_dpp v44, v44, v44 row_shr:1 row_mask:0xf bank_mask:0xf
	s_nop 1
	v_max_f32_dpp v44, v44, v44 row_shr:2 row_mask:0xf bank_mask:0xf
	s_nop 1
	v_max_f32_dpp v44, v44, v44 row_shr:4 row_mask:0xf bank_mask:0xf
	s_nop 1
	v_max_f32_dpp v44, v44, v44 row_shr:8 row_mask:0xf bank_mask:0xf
	s_nop 1
	v_max_f32_dpp v44, v44, v44 row_bcast:15 row_mask:0xa bank_mask:0xf
	s_nop 1
	v_max_f32_dpp v44, v44, v44 row_bcast:31 row_mask:0xc bank_mask:0xf
	s_nop 1
	v_readlane_b32 s14, v44, 63
	s_nop 1
	v_subrev_f32_e32 v46, s14, v10
	v_subrev_f32_e32 v47, s14, v12
	v_subrev_f32_e32 v48, s14, v14
	v_subrev_f32_e32 v49, s14, v16
	v_mul_f32_e32 v46, 0x3fb8aa3b, v46
	v_mul_f32_e32 v47, 0x3fb8aa3b, v47
	v_mul_f32_e32 v48, 0x3fb8aa3b, v48
	v_mul_f32_e32 v49, 0x3fb8aa3b, v49
	v_exp_f32_e32 v46, v46
	v_exp_f32_e32 v47, v47
	v_exp_f32_e32 v48, v48
	v_exp_f32_e32 v49, v49
	s_nop 0
	v_mul_f32_e32 v50, v11, v46
	v_fmac_f32_e32 v50, v13, v47
	v_fmac_f32_e32 v50, v15, v48
	v_fmac_f32_e32 v50, v17, v49
	s_waitcnt vmcnt(2)
	v_mul_f32_e32 v52, v46, v20
	v_mul_f32_e32 v53, v46, v24
	v_mul_f32_e32 v54, v46, v28
	v_mul_f32_e32 v55, v46, v32
	v_fmac_f32_e32 v52, v47, v21
	v_fmac_f32_e32 v53, v47, v25
	v_fmac_f32_e32 v54, v47, v29
	v_fmac_f32_e32 v55, v47, v33
	v_fmac_f32_e32 v52, v48, v22
	v_fmac_f32_e32 v53, v48, v26
	v_fmac_f32_e32 v54, v48, v30
	v_fmac_f32_e32 v55, v48, v34
	v_fmac_f32_e32 v52, v49, v23
	v_fmac_f32_e32 v53, v49, v27
	v_fmac_f32_e32 v54, v49, v31
	v_fmac_f32_e32 v55, v49, v35
	v_add_f32_dpp v50, v50, v50 row_shr:1 row_mask:0xf bank_mask:0xf
	v_add_f32_dpp v52, v52, v52 row_shr:1 row_mask:0xf bank_mask:0xf
	v_add_f32_dpp v53, v53, v53 row_shr:1 row_mask:0xf bank_mask:0xf
	v_add_f32_dpp v54, v54, v54 row_shr:1 row_mask:0xf bank_mask:0xf
	v_add_f32_dpp v55, v55, v55 row_shr:1 row_mask:0xf bank_mask:0xf
	v_add_f32_dpp v50, v50, v50 row_shr:2 row_mask:0xf bank_mask:0xf
	v_add_f32_dpp v52, v52, v52 row_shr:2 row_mask:0xf bank_mask:0xf
	v_add_f32_dpp v53, v53, v53 row_shr:2 row_mask:0xf bank_mask:0xf
	v_add_f32_dpp v54, v54, v54 row_shr:2 row_mask:0xf bank_mask:0xf
	v_add_f32_dpp v55, v55, v55 row_shr:2 row_mask:0xf bank_mask:0xf
	v_add_f32_dpp v50, v50, v50 row_shr:4 row_mask:0xf bank_mask:0xf
	v_add_f32_dpp v52, v52, v52 row_shr:4 row_mask:0xf bank_mask:0xf
	v_add_f32_dpp v53, v53, v53 row_shr:4 row_mask:0xf bank_mask:0xf
	v_add_f32_dpp v54, v54, v54 row_shr:4 row_mask:0xf bank_mask:0xf
	v_add_f32_dpp v55, v55, v55 row_shr:4 row_mask:0xf bank_mask:0xf
	v_add_f32_dpp v50, v50, v50 row_shr:8 row_mask:0xf bank_mask:0xf
	v_add_f32_dpp v52, v52, v52 row_shr:8 row_mask:0xf bank_mask:0xf
	v_add_f32_dpp v53, v53, v53 row_shr:8 row_mask:0xf bank_mask:0xf
	v_add_f32_dpp v54, v54, v54 row_shr:8 row_mask:0xf bank_mask:0xf
	v_add_f32_dpp v55, v55, v55 row_shr:8 row_mask:0xf bank_mask:0xf
	v_add_f32_dpp v50, v50, v50 row_bcast:15 row_mask:0xa bank_mask:0xf
	v_add_f32_dpp v52, v52, v52 row_bcast:15 row_mask:0xa bank_mask:0xf
	v_add_f32_dpp v53, v53, v53 row_bcast:15 row_mask:0xa bank_mask:0xf
	v_add_f32_dpp v54, v54, v54 row_bcast:15 row_mask:0xa bank_mask:0xf
	v_add_f32_dpp v55, v55, v55 row_bcast:15 row_mask:0xa bank_mask:0xf
	v_add_f32_dpp v50, v50, v50 row_bcast:31 row_mask:0xc bank_mask:0xf
	v_add_f32_dpp v52, v52, v52 row_bcast:31 row_mask:0xc bank_mask:0xf
	v_add_f32_dpp v53, v53, v53 row_bcast:31 row_mask:0xc bank_mask:0xf
	v_add_f32_dpp v54, v54, v54 row_bcast:31 row_mask:0xc bank_mask:0xf
	v_add_f32_dpp v55, v55, v55 row_bcast:31 row_mask:0xc bank_mask:0xf
	s_nop 1
	v_readlane_b32 s15, v50, 63
	v_readlane_b32 s16, v52, 63
	v_readlane_b32 s17, v53, 63
	v_readlane_b32 s18, v54, 63
	v_readlane_b32 s19, v55, 63
	s_nop 1
	v_mov_b32_e32 v56, s15
	v_rcp_f32_e32 v56, v56
	s_nop 0
	v_mul_f32_e32 v57, s16, v56
	v_mul_f32_e32 v58, s17, v56
	v_mul_f32_e32 v59, s18, v56
	v_mul_f32_e32 v60, s19, v56
	s_waitcnt vmcnt(0)
	v_mul_f32_e32 v61, v36, v57
	v_mul_f32_e32 v62, v40, v57
	v_fmac_f32_e32 v61, v37, v58
	v_fmac_f32_e32 v62, v41, v58
	v_fmac_f32_e32 v61, v38, v59
	v_fmac_f32_e32 v62, v42, v59
	v_fmac_f32_e32 v61, v39, v60
	v_fmac_f32_e32 v62, v43, v60
	v_lshl_add_u32 v9, v2, 9, v8
	ds_write_b32 v9, v61
	ds_write_b32 v9, v62 offset:256
	v_readfirstlane_b32 s20, v2
	s_waitcnt lgkmcnt(0)
	s_barrier
	s_cmp_lg_u32 s20, 0
	s_cbranch_scc1 .Lp3_done
	ds_read_b32 v61, v8
	ds_read_b32 v62, v8 offset:256
	ds_read_b32 v52, v8 offset:512
	ds_read_b32 v53, v8 offset:768
	ds_read_b32 v54, v8 offset:1024
	ds_read_b32 v55, v8 offset:1280
	ds_read_b32 v56, v8 offset:1536
	ds_read_b32 v57, v8 offset:1792
	s_waitcnt lgkmcnt(4)
	v_add_f32_e32 v61, v61, v52
	v_add_f32_e32 v62, v62, v53
	s_waitcnt lgkmcnt(2)
	v_add_f32_e32 v61, v61, v54
	v_add_f32_e32 v62, v62, v55
	s_waitcnt lgkmcnt(0)
	v_add_f32_e32 v61, v61, v56
	v_add_f32_e32 v62, v62, v57
	global_atomic_add_f32 v8, v61, s[8:9]
	global_atomic_add_f32 v8, v62, s[8:9] offset:256

	.amdhsa_kernel _Z12pool3_kernelPKfS0_Pf
		.amdhsa_group_segment_fixed_size 18592
		.amdhsa_private_segment_fixed_size 0
		.amdhsa_kernarg_size 24
		.amdhsa_user_sgpr_count 2
		.amdhsa_user_sgpr_dispatch_ptr 0
		.amdhsa_user_sgpr_queue_ptr 0
		.amdhsa_user_sgpr_kernarg_segment_ptr 1
		.amdhsa_user_sgpr_dispatch_id 0
		.amdhsa_user_sgpr_kernarg_preload_length 0
		.amdhsa_user_sgpr_kernarg_preload_offset 0
		.amdhsa_user_sgpr_private_segment_size 0
		.amdhsa_uses_dynamic_stack 0
		.amdhsa_enable_private_segment 0
		.amdhsa_system_sgpr_workgroup_id_x 1
		.amdhsa_system_sgpr_workgroup_id_y 0
		.amdhsa_system_sgpr_workgroup_id_z 0
		.amdhsa_system_sgpr_workgroup_info 0
		.amdhsa_system_vgpr_workitem_id 0
		.amdhsa_next_free_vgpr 64
		.amdhsa_next_free_sgpr 24
		.amdhsa_accum_offset 64
		.amdhsa_reserve_vcc 1
		.amdhsa_float_round_mode_32 0
		.amdhsa_float_round_mode_16_64 0
		.amdhsa_float_denorm_mode_32 3
		.amdhsa_float_denorm_mode_16_64 3
		.amdhsa_dx10_clamp 1
		.amdhsa_ieee_mode 1
		.amdhsa_fp16_overflow 0
		.amdhsa_tg_split 0
		.amdhsa_exception_fp_ieee_invalid_op 0
		.amdhsa_exception_fp_denorm_src 0
		.amdhsa_exception_fp_ieee_div_zero 0
		.amdhsa_exception_fp_ieee_overflow 0
		.amdhsa_exception_fp_ieee_underflow 0
		.amdhsa_exception_fp_ieee_inexact 0
		.amdhsa_exception_int_div_zero 0
	.end_amdhsa_kernel

.Lfunc_end1:
	.size	_Z12pool3_kernelPKfS0_Pf, .Lfunc_end1-_Z12pool3_kernelPKfS0_Pf
	.set _Z12pool3_kernelPKfS0_Pf.num_vgpr, 64
	.set _Z12pool3_kernelPKfS0_Pf.num_agpr, 0
	.set _Z12pool3_kernelPKfS0_Pf.numbered_sgpr, 24
	.set _Z12pool3_kernelPKfS0_Pf.num_named_barrier, 0
	.set _Z12pool3_kernelPKfS0_Pf.private_seg_size, 0
	.set _Z12pool3_kernelPKfS0_Pf.uses_vcc, 1
	.set _Z12pool3_kernelPKfS0_Pf.uses_flat_scratch, 0
	.set _Z12pool3_kernelPKfS0_Pf.has_dyn_sized_stack, 0
	.set _Z12pool3_kernelPKfS0_Pf.has_recursion, 0
	.set _Z12pool3_kernelPKfS0_Pf.has_indirect_call, 0

amdhsa.kernels:
  - .agpr_count:     0
    .args:
      - .actual_access:  read_only
        .address_space:  global
        .offset:         0
        .size:           8
        .value_kind:     global_buffer
      - .actual_access:  read_only
        .address_space:  global
        .offset:         8
        .size:           8
        .value_kind:     global_buffer
      - .actual_access:  read_only
        .address_space:  global
        .offset:         16
        .size:           8
        .value_kind:     global_buffer
      - .actual_access:  read_only
        .address_space:  global
        .offset:         24
        .size:           8
        .value_kind:     global_buffer
      - .actual_access:  read_only
        .address_space:  global
        .offset:         32
        .size:           8
        .value_kind:     global_buffer
      - .actual_access:  read_only
        .address_space:  global
        .offset:         40
        .size:           8
        .value_kind:     global_buffer
      - .actual_access:  read_only
        .address_space:  global
        .offset:         48
        .size:           8
        .value_kind:     global_buffer
      - .actual_access:  read_only
        .address_space:  global
        .offset:         56
        .size:           8
        .value_kind:     global_buffer
      - .actual_access:  read_only
        .address_space:  global
        .offset:         64
        .size:           8
        .value_kind:     global_buffer
      - .actual_access:  read_only
        .address_space:  global
        .offset:         72
        .size:           8
        .value_kind:     global_buffer
      - .actual_access:  write_only
        .address_space:  global
        .offset:         80
        .size:           8
        .value_kind:     global_buffer
      - .actual_access:  write_only
        .address_space:  global
        .offset:         88
        .size:           8
        .value_kind:     global_buffer
    .group_segment_fixed_size: 161344
    .kernarg_segment_align: 8
    .kernarg_segment_size: 96
    .language:       OpenCL C
    .language_version:
      - 2
      - 0
    .max_flat_workgroup_size: 512
    .name:           _Z12pool1_kernelPKfS0_S0_S0_S0_S0_S0_S0_S0_S0_PfS1_
    .private_segment_fixed_size: 0
    .sgpr_count:     42
    .sgpr_spill_count: 0
    .symbol:         _Z12pool1_kernelPKfS0_S0_S0_S0_S0_S0_S0_S0_S0_PfS1_.kd
    .uniform_work_group_size: 1
    .uses_dynamic_stack: false
    .vgpr_count:     256
    .vgpr_spill_count: 0
    .wavefront_size: 64
  - .agpr_count:     0
    .args:
      - .actual_access:  read_only
        .address_space:  global
        .offset:         0
        .size:           8
        .value_kind:     global_buffer
      - .actual_access:  read_only
        .address_space:  global
        .offset:         8
        .size:           8
        .value_kind:     global_buffer
      - .address_space:  global
        .offset:         16
        .size:           8
        .value_kind:     global_buffer
    .group_segment_fixed_size: 18592
    .kernarg_segment_align: 8
    .kernarg_segment_size: 24
    .language:       OpenCL C
    .language_version:
      - 2
      - 0
    .max_flat_workgroup_size: 256
    .name:           _Z12pool3_kernelPKfS0_Pf
    .private_segment_fixed_size: 0
    .sgpr_count:     30
    .sgpr_spill_count: 0
    .symbol:         _Z12pool3_kernelPKfS0_Pf.kd
    .uniform_work_group_size: 1
    .uses_dynamic_stack: false
    .vgpr_count:     64
    .vgpr_spill_count: 0
    .wavefront_size: 64
